# v55 + prologue de-serialisation: in the proj, out-proj and down phases the second group of prologue DMA loads (K-tile 1) is issued before the first counted wait (vmcnt(8)) instead of behind it
# baseline (speedup 1.0000x reference)
; #define PG8_LAS __attribute__((address_space(3)))
; #define PG8_STAGE(bufoff, gbase, voff) do { _Pragma("unroll") for (int _i = 0; _i < 2; ++_i) \
;         __builtin_amdgcn_global_load_lds((const unsigned*)((const char*)(gbase) + (voff)[_i]), (PG8_LAS unsigned*)(lds + (bufoff) + ldsw + _i * 8192), 16, 0, 0); } while (0)
; #define PG8_WAIT_V(n) asm volatile("s_waitcnt vmcnt(" #n ")" ::: "memory")
; #define PG8_BAR __builtin_amdgcn_s_barrier()
; template <class Epi, class Sched, bool ALIGN_EPI = false, bool SP2 = false>
; __device__ __forceinline__ void gemm_phase(PG8_LAS unsigned char* lds, const Gemm g, const Sched& S, const Epi& E) {
;     ...
;     f32x4 acc[2][2][4][2];
; #pragma unroll
;     for (int a = 0; a < 2; ++a)
; #pragma unroll
;         for (int b = 0; b < 2; ++b)
; #pragma unroll
;             for (int m = 0; m < 4; ++m)
; #pragma unroll
;                 for (int n = 0; n < 2; ++n) acc[a][b][m][n] = (f32x4){0.f, 0.f, 0.f, 0.f};
;     ...
;         PG8_STAGE(PG8_SB(0, 0), cB, voffB); PG8_STAGE(PG8_SB(0, 1), cB + hstep, voffB); PG8_STAGE(PG8_SA(0, 0), cA, voffA); PG8_STAGE(PG8_SA(0, 1), cA + hstep, voffA);
;         if (wr == 1) PG8_BAR;
;         PG8_WAIT_V(2); PG8_BAR;
;         if constexpr (Epi::ROWSCALE) stage_row_factors(rowp_, (PG8_LAS float*)E.rsl, tid);
;         PG8_STAGE(PG8_SB(1, 0), cB + kstep, voffB); PG8_STAGE(PG8_SA(1, 0), cA + kstep, voffA); PG8_STAGE(PG8_SB(1, 1), cB + hstep + kstep, voffB);
;         PG8_WAIT_V(6); PG8_BAR;
.LBB0_1125:
	s_add_u32 s34, s12, 0x10000000
	s_addc_u32 s35, s13, 0
	s_add_u32 s10, s12, 0x11000000
	s_addc_u32 s11, s13, 0
	s_add_u32 s12, s12, 0x12000000
	s_addc_u32 s13, s13, 0
	s_lshl_b32 s5, s18, 5
	s_and_b32 s5, s5, 0x60
	s_add_i32 m0, s28, 0x18000
	v_lshl_add_u64 v[10:11], v[10:11], 0, s[42:43]
	s_lshl_b32 s1, s17, 13
	s_waitcnt lgkmcnt(0)
	s_lshl_b32 s20, s5, 7
	global_load_lds_dwordx4 v[10:11], off
	v_lshl_add_u64 v[8:9], v[8:9], 0, s[42:43]
	s_add_i32 m0, s28, 0x1a000
	s_add_i32 s36, s28, 0x8000
	s_add_i32 s40, s28, 0xa000
	global_load_lds_dwordx4 v[8:9], off
	v_lshl_add_u64 v[4:5], v[4:5], 0, s[42:43]
	s_mov_b32 m0, s36
	s_add_u32 s18, s14, 0x20080
	global_load_lds_dwordx4 v[4:5], off
	v_lshl_add_u64 v[4:5], v[6:7], 0, s[42:43]
	s_mov_b32 m0, s40
	s_addc_u32 s19, s15, 0
	global_load_lds_dwordx4 v[4:5], off
	s_add_i32 m0, s28, 0x1c000
	v_lshl_add_u64 v[4:5], s[18:19], 0, v[2:3]
	global_load_lds_dwordx4 v[4:5], off
	v_lshl_add_u64 v[4:5], s[18:19], 0, v[168:169]
	s_add_i32 m0, s28, 0x1e000
	v_mov_b32_e32 v7, v3
	global_load_lds_dwordx4 v[4:5], off
	s_waitcnt vmcnt(8)
	s_barrier
	v_lshrrev_b32_e32 v5, 1, v12
	v_and_b32_e32 v5, 24, v5
	v_and_b32_e32 v4, 15, v12
	v_lshlrev_b32_e32 v6, 1, v5
	v_lshl_or_b32 v200, s17, 6, v4
	v_lshl_or_b32 v4, v4, 6, v6
	v_lshlrev_b32_e32 v6, 2, v12
	v_and_b32_e32 v6, 32, v6
	v_bitop3_b32 v8, v4, s1, v6 bitop3:0xde
	v_bitop3_b32 v201, v4, s20, v6 bitop3:0xde
	v_lshlrev_b32_e32 v4, 13, v13
	v_and_b32_e32 v4, 0xffffc000, v4
	v_or_b32_e32 v202, s5, v5
	v_lshl_add_u32 v4, v14, 10, v4
	v_and_b32_e32 v5, 1, v13
	v_lshl_or_b32 v4, v5, 6, v4
	v_lshl_add_u32 v170, v15, 1, v4
	v_lshlrev_b32_e32 v4, 13, v16
	v_and_b32_e32 v4, 0xffffc000, v4
	v_lshl_add_u32 v4, v17, 10, v4
	v_and_b32_e32 v5, 1, v16
	s_waitcnt vmcnt(6)
	v_lshl_or_b32 v4, v5, 6, v4
	v_mov_b32_e32 v6, v3
	s_cmpk_lt_u32 s16, 0x100
	v_lshl_add_u32 v172, v18, 1, v4
	v_mov_b32_e32 v4, v3
	v_mov_b32_e32 v5, v3
	v_add_u32_e32 v203, 0, v8
	v_mov_b64_e32 v[10:11], v[6:7]
	v_mov_b64_e32 v[22:23], v[6:7]
	v_mov_b64_e32 v[26:27], v[6:7]
	v_mov_b64_e32 v[46:47], v[6:7]
	v_mov_b64_e32 v[50:51], v[6:7]
	v_mov_b64_e32 v[78:79], v[6:7]
	v_mov_b64_e32 v[82:83], v[6:7]
	v_mov_b64_e32 v[14:15], v[6:7]
	v_mov_b64_e32 v[18:19], v[6:7]
	v_mov_b64_e32 v[30:31], v[6:7]
	v_mov_b64_e32 v[34:35], v[6:7]
	v_mov_b64_e32 v[62:63], v[6:7]
	v_mov_b64_e32 v[66:67], v[6:7]
	v_mov_b64_e32 v[94:95], v[6:7]
	v_mov_b64_e32 v[98:99], v[6:7]
	v_mov_b64_e32 v[110:111], v[6:7]
	v_mov_b64_e32 v[114:115], v[6:7]
	v_mov_b64_e32 v[142:143], v[6:7]
	v_mov_b64_e32 v[146:147], v[6:7]
	v_mov_b64_e32 v[150:151], v[6:7]
	v_mov_b64_e32 v[154:155], v[6:7]
	v_mov_b64_e32 v[158:159], v[6:7]
	v_mov_b64_e32 v[162:163], v[6:7]
	v_mov_b64_e32 v[126:127], v[6:7]
	v_mov_b64_e32 v[130:131], v[6:7]
	v_mov_b64_e32 v[118:119], v[6:7]
	v_mov_b64_e32 v[122:123], v[6:7]
	v_mov_b64_e32 v[86:87], v[6:7]
	v_mov_b64_e32 v[90:91], v[6:7]
	v_mov_b64_e32 v[54:55], v[6:7]
	v_mov_b64_e32 v[58:59], v[6:7]
	s_cselect_b64 s[16:17], -1, 0
	v_mov_b32_e32 v171, v3
	v_mov_b32_e32 v173, v3
	s_mov_b32 s1, 0
	v_mov_b64_e32 v[8:9], v[4:5]
	v_mov_b64_e32 v[20:21], v[4:5]
	v_mov_b64_e32 v[24:25], v[4:5]
	v_mov_b64_e32 v[44:45], v[4:5]
	v_mov_b64_e32 v[48:49], v[4:5]
	v_mov_b64_e32 v[76:77], v[4:5]
	v_mov_b64_e32 v[80:81], v[4:5]
	v_mov_b64_e32 v[12:13], v[4:5]
	v_mov_b64_e32 v[16:17], v[4:5]
	v_mov_b64_e32 v[28:29], v[4:5]
	v_mov_b64_e32 v[32:33], v[4:5]
	v_mov_b64_e32 v[60:61], v[4:5]
	v_mov_b64_e32 v[64:65], v[4:5]
	v_mov_b64_e32 v[92:93], v[4:5]
	v_mov_b64_e32 v[96:97], v[4:5]
	v_mov_b64_e32 v[108:109], v[4:5]
	v_mov_b64_e32 v[112:113], v[4:5]
	v_mov_b64_e32 v[140:141], v[4:5]
	v_mov_b64_e32 v[144:145], v[4:5]
	v_mov_b64_e32 v[148:149], v[4:5]
	v_mov_b64_e32 v[152:153], v[4:5]
	v_mov_b64_e32 v[156:157], v[4:5]
	v_mov_b64_e32 v[160:161], v[4:5]
	v_mov_b64_e32 v[124:125], v[4:5]
	v_mov_b64_e32 v[128:129], v[4:5]
	v_mov_b64_e32 v[116:117], v[4:5]
	v_mov_b64_e32 v[120:121], v[4:5]
	v_mov_b64_e32 v[84:85], v[4:5]
	v_mov_b64_e32 v[88:89], v[4:5]
	v_mov_b64_e32 v[52:53], v[4:5]
	v_mov_b64_e32 v[56:57], v[4:5]
	s_barrier
	s_branch .LBB0_1128
	.p2align 6
	s_nop 0
	s_nop 0
	s_nop 0
	s_nop 0
	s_nop 0
	s_nop 0
	s_nop 0
	s_nop 0
	s_nop 0
	s_nop 0

; #define PG8_LAS __attribute__((address_space(3)))
; #define PG8_STAGE(bufoff, gbase, voff) do { _Pragma("unroll") for (int _i = 0; _i < 2; ++_i) \
;         __builtin_amdgcn_global_load_lds((const unsigned*)((const char*)(gbase) + (voff)[_i]), (PG8_LAS unsigned*)(lds + (bufoff) + ldsw + _i * 8192), 16, 0, 0); } while (0)
; #define PG8_WAIT_V(n) asm volatile("s_waitcnt vmcnt(" #n ")" ::: "memory")
; #define PG8_BAR __builtin_amdgcn_s_barrier()
; template <class Epi, class Sched, bool ALIGN_EPI = false, bool SP2 = false>
; __device__ __forceinline__ void gemm_phase(PG8_LAS unsigned char* lds, const Gemm g, const Sched& S, const Epi& E) {
;     ...
;     f32x4 acc[2][2][4][2];
; #pragma unroll
;     for (int a = 0; a < 2; ++a)
; #pragma unroll
;         for (int b = 0; b < 2; ++b)
; #pragma unroll
;             for (int m = 0; m < 4; ++m)
; #pragma unroll
;                 for (int n = 0; n < 2; ++n) acc[a][b][m][n] = (f32x4){0.f, 0.f, 0.f, 0.f};
;     ...
;         PG8_STAGE(PG8_SB(0, 0), cB, voffB); PG8_STAGE(PG8_SB(0, 1), cB + hstep, voffB); PG8_STAGE(PG8_SA(0, 0), cA, voffA); PG8_STAGE(PG8_SA(0, 1), cA + hstep, voffA);
;         if (wr == 1) PG8_BAR;
;         PG8_WAIT_V(2); PG8_BAR;
;         if constexpr (Epi::ROWSCALE) stage_row_factors(rowp_, (PG8_LAS float*)E.rsl, tid);
;         PG8_STAGE(PG8_SB(1, 0), cB + kstep, voffB); PG8_STAGE(PG8_SA(1, 0), cA + kstep, voffA); PG8_STAGE(PG8_SB(1, 1), cB + hstep + kstep, voffB);
;         PG8_WAIT_V(6); PG8_BAR;
.LBB0_1292:
	v_lshl_add_u64 v[10:11], s[0:1], 0, v[2:3]
	v_mov_b32_e32 v137, v3
	v_and_b32_e32 v147, 15, v146
	v_and_b32_e32 v18, 48, v146
	v_lshlrev_b32_e32 v19, 2, v146
	v_lshl_add_u64 v[12:13], s[0:1], 0, v[136:137]
	v_mov_b32_e32 v133, v3
	s_sext_i32_i8 s16, s6
	s_and_b32 s23, s17, 3
	s_lshl_b32 s6, s22, 13
	v_lshl_or_b32 v18, v147, 6, v18
	v_and_b32_e32 v19, 32, v19
	s_add_i32 m0, s40, 0x18000
	v_lshl_add_u64 v[10:11], v[10:11], 0, s[42:43]
	v_lshl_add_u64 v[14:15], s[4:5], 0, v[132:133]
	v_mov_b32_e32 v135, v3
	s_lshl_b32 s9, s22, 6
	v_bitop3_b32 v20, v18, s6, v19 bitop3:0xde
	s_lshl_b32 s6, s23, 12
	global_load_lds_dwordx4 v[10:11], off
	v_lshl_add_u64 v[10:11], v[12:13], 0, s[42:43]
	s_add_i32 m0, s40, 0x1a000
	s_add_i32 s58, s40, 0x8000
	s_add_i32 s59, s40, 0xa000
	v_lshl_add_u64 v[16:17], s[4:5], 0, v[134:135]
	v_bitop3_b32 v148, v18, s6, v19 bitop3:0xde
	global_load_lds_dwordx4 v[10:11], off
	v_lshl_add_u64 v[10:11], v[14:15], 0, s[42:43]
	s_mov_b32 m0, s58
	s_add_u32 s6, s0, 0x40080
	global_load_lds_dwordx4 v[10:11], off
	v_lshl_add_u64 v[10:11], v[16:17], 0, s[42:43]
	s_mov_b32 m0, s59
	s_addc_u32 s7, s1, 0
	global_load_lds_dwordx4 v[10:11], off
	s_add_i32 m0, s40, 0x1c000
	v_lshl_add_u64 v[10:11], s[6:7], 0, v[2:3]
	global_load_lds_dwordx4 v[10:11], off
	v_lshl_add_u64 v[10:11], s[6:7], 0, v[136:137]
	s_add_i32 m0, s40, 0x1e000
	v_or_b32_e32 v214, s9, v147
	global_load_lds_dwordx4 v[10:11], off
	s_waitcnt vmcnt(8)
	s_barrier
	v_lshlrev_b32_e32 v10, 14, v4
	v_and_b32_e32 v10, 0xffff8000, v10
	v_lshl_add_u32 v5, v5, 11, v10
	v_and_b32_e32 v4, 1, v4
	v_lshl_or_b32 v4, v4, 6, v5
	v_lshl_add_u32 v138, v6, 1, v4
	v_lshlrev_b32_e32 v4, 14, v7
	v_and_b32_e32 v4, 0xffff8000, v4
	v_lshl_add_u32 v4, v8, 11, v4
	v_and_b32_e32 v5, 1, v7
	s_waitcnt vmcnt(6)
	v_lshl_or_b32 v4, v5, 6, v4
	v_lshl_add_u32 v140, v9, 1, v4
	v_mov_b32_e32 v4, 0
	v_mov_b32_e32 v139, v3
	v_mov_b32_e32 v141, v3
	s_mov_b32 s60, 0
	v_add_u32_e32 v149, 0, v20
	v_mov_b32_e32 v5, v4
	v_mov_b32_e32 v6, v4
	v_mov_b32_e32 v7, v4
	v_mov_b32_e32 v8, v4
	v_mov_b32_e32 v9, v4
	v_mov_b32_e32 v10, v4
	v_mov_b32_e32 v11, v4
	v_mov_b32_e32 v20, v4
	v_mov_b32_e32 v21, v4
	v_mov_b32_e32 v22, v4
	v_mov_b32_e32 v23, v4
	v_mov_b32_e32 v24, v4
	v_mov_b32_e32 v25, v4
	v_mov_b32_e32 v26, v4
	v_mov_b32_e32 v27, v4
	v_mov_b32_e32 v36, v4
	v_mov_b32_e32 v37, v4
	v_mov_b32_e32 v38, v4
	v_mov_b32_e32 v39, v4
	v_mov_b32_e32 v40, v4
	v_mov_b32_e32 v41, v4
	v_mov_b32_e32 v42, v4
	v_mov_b32_e32 v43, v4
	v_mov_b32_e32 v52, v4
	v_mov_b32_e32 v53, v4
	v_mov_b32_e32 v54, v4
	v_mov_b32_e32 v55, v4
	v_mov_b32_e32 v56, v4
	v_mov_b32_e32 v57, v4
	v_mov_b32_e32 v58, v4
	v_mov_b32_e32 v59, v4
	v_mov_b32_e32 v12, v4
	v_mov_b32_e32 v13, v4
	v_mov_b32_e32 v14, v4
	v_mov_b32_e32 v15, v4
	v_mov_b32_e32 v16, v4
	v_mov_b32_e32 v17, v4
	v_mov_b32_e32 v18, v4
	v_mov_b32_e32 v19, v4
	v_mov_b32_e32 v28, v4
	v_mov_b32_e32 v29, v4
	s_waitcnt lgkmcnt(0)
	v_mov_b32_e32 v30, v4
	v_mov_b32_e32 v31, v4
	v_mov_b32_e32 v32, v4
	v_mov_b32_e32 v33, v4
	v_mov_b32_e32 v34, v4
	v_mov_b32_e32 v35, v4
	v_mov_b32_e32 v44, v4
	v_mov_b32_e32 v45, v4
	v_mov_b32_e32 v46, v4
	v_mov_b32_e32 v47, v4
	v_mov_b32_e32 v48, v4
	v_mov_b32_e32 v49, v4
	v_mov_b32_e32 v50, v4
	v_mov_b32_e32 v51, v4
	v_mov_b32_e32 v60, v4
	v_mov_b32_e32 v61, v4
	v_mov_b32_e32 v62, v4
	v_mov_b32_e32 v63, v4
	v_mov_b32_e32 v64, v4
	v_mov_b32_e32 v65, v4
	v_mov_b32_e32 v66, v4
	v_mov_b32_e32 v67, v4
	v_mov_b32_e32 v68, v4
	v_mov_b32_e32 v69, v4
	v_mov_b32_e32 v70, v4
	v_mov_b32_e32 v71, v4
	v_mov_b32_e32 v72, v4
	v_mov_b32_e32 v73, v4
	v_mov_b32_e32 v74, v4
	v_mov_b32_e32 v75, v4
	v_mov_b32_e32 v84, v4
	v_mov_b32_e32 v85, v4
	v_mov_b32_e32 v86, v4
	v_mov_b32_e32 v87, v4
	v_mov_b32_e32 v88, v4
	v_mov_b32_e32 v89, v4
	v_mov_b32_e32 v90, v4
	v_mov_b32_e32 v91, v4
	v_mov_b32_e32 v100, v4
	v_mov_b32_e32 v101, v4
	v_mov_b32_e32 v102, v4
	v_mov_b32_e32 v103, v4
	v_mov_b32_e32 v104, v4
	v_mov_b32_e32 v105, v4
	v_mov_b32_e32 v106, v4
	v_mov_b32_e32 v107, v4
	v_mov_b32_e32 v116, v4
	v_mov_b32_e32 v117, v4
	v_mov_b32_e32 v118, v4
	v_mov_b32_e32 v119, v4
	v_mov_b32_e32 v120, v4
	v_mov_b32_e32 v121, v4
	v_mov_b32_e32 v122, v4
	v_mov_b32_e32 v123, v4
	v_mov_b32_e32 v76, v4
	v_mov_b32_e32 v77, v4
	v_mov_b32_e32 v78, v4
	v_mov_b32_e32 v79, v4
	v_mov_b32_e32 v80, v4
	v_mov_b32_e32 v81, v4
	v_mov_b32_e32 v82, v4
	v_mov_b32_e32 v83, v4
	v_mov_b32_e32 v92, v4
	v_mov_b32_e32 v93, v4
	v_mov_b32_e32 v94, v4
	v_mov_b32_e32 v95, v4
	v_mov_b32_e32 v96, v4
	v_mov_b32_e32 v97, v4
	v_mov_b32_e32 v98, v4
	v_mov_b32_e32 v99, v4
	v_mov_b32_e32 v108, v4
	v_mov_b32_e32 v109, v4
	v_mov_b32_e32 v110, v4
	v_mov_b32_e32 v111, v4
	v_mov_b32_e32 v112, v4
	v_mov_b32_e32 v113, v4
	v_mov_b32_e32 v114, v4
	v_mov_b32_e32 v115, v4
	v_mov_b32_e32 v124, v4
	v_mov_b32_e32 v125, v4
	v_mov_b32_e32 v126, v4
	v_mov_b32_e32 v127, v4
	v_mov_b32_e32 v128, v4
	v_mov_b32_e32 v129, v4
	v_mov_b32_e32 v130, v4
	v_mov_b32_e32 v131, v4
	s_barrier

; #define PG8_LAS __attribute__((address_space(3)))
; #define PG8_STAGE(bufoff, gbase, voff) do { _Pragma("unroll") for (int _i = 0; _i < 2; ++_i) \
;         __builtin_amdgcn_global_load_lds((const unsigned*)((const char*)(gbase) + (voff)[_i]), (PG8_LAS unsigned*)(lds + (bufoff) + ldsw + _i * 8192), 16, 0, 0); } while (0)
; #define PG8_WAIT_V(n) asm volatile("s_waitcnt vmcnt(" #n ")" ::: "memory")
; #define PG8_BAR __builtin_amdgcn_s_barrier()
; template <class Epi, class Sched, bool ALIGN_EPI = false, bool SP2 = false>
; __device__ __forceinline__ void gemm_phase(PG8_LAS unsigned char* lds, const Gemm g, const Sched& S, const Epi& E) {
;     ...
;     f32x4 acc[2][2][4][2];
; #pragma unroll
;     for (int a = 0; a < 2; ++a)
; #pragma unroll
;         for (int b = 0; b < 2; ++b)
; #pragma unroll
;             for (int m = 0; m < 4; ++m)
; #pragma unroll
;                 for (int n = 0; n < 2; ++n) acc[a][b][m][n] = (f32x4){0.f, 0.f, 0.f, 0.f};
;     ...
;         PG8_STAGE(PG8_SB(0, 0), cB, voffB); PG8_STAGE(PG8_SB(0, 1), cB + hstep, voffB); PG8_STAGE(PG8_SA(0, 0), cA, voffA); PG8_STAGE(PG8_SA(0, 1), cA + hstep, voffA);
;         if (wr == 1) PG8_BAR;
;         PG8_WAIT_V(2); PG8_BAR;
;         if constexpr (Epi::ROWSCALE) stage_row_factors(rowp_, (PG8_LAS float*)E.rsl, tid);
;         PG8_STAGE(PG8_SB(1, 0), cB + kstep, voffB); PG8_STAGE(PG8_SA(1, 0), cA + kstep, voffA); PG8_STAGE(PG8_SB(1, 1), cB + hstep + kstep, voffB);
;         PG8_WAIT_V(6); PG8_BAR;
.LBB0_1768:
	s_lshr_b32 s4, s4, 3
	v_lshl_add_u64 v[12:13], s[0:1], 0, v[2:3]
	v_mov_b32_e32 v137, v3
	v_and_b32_e32 v147, 15, v146
	v_and_b32_e32 v20, 48, v146
	v_lshlrev_b32_e32 v21, 2, v146
	v_lshl_add_u64 v[14:15], s[0:1], 0, v[136:137]
	v_mov_b32_e32 v133, v3
	s_sext_i32_i8 s16, s4
	s_and_b32 s25, s17, 3
	s_lshl_b32 s4, s22, 13
	v_lshl_or_b32 v20, v147, 6, v20
	v_and_b32_e32 v21, 32, v21
	s_add_i32 m0, s35, 0x18000
	v_lshl_add_u64 v[12:13], v[12:13], 0, s[42:43]
	v_lshl_add_u64 v[16:17], s[6:7], 0, v[132:133]
	v_mov_b32_e32 v135, v3
	s_lshl_b32 s24, s22, 6
	v_bitop3_b32 v22, v20, s4, v21 bitop3:0xde
	s_lshl_b32 s4, s25, 12
	global_load_lds_dwordx4 v[12:13], off
	v_lshl_add_u64 v[12:13], v[14:15], 0, s[42:43]
	s_add_i32 m0, s35, 0x1a000
	s_add_i32 s40, s35, 0x8000
	s_add_i32 s41, s35, 0xa000
	v_lshl_add_u64 v[18:19], s[6:7], 0, v[134:135]
	v_bitop3_b32 v148, v20, s4, v21 bitop3:0xde
	global_load_lds_dwordx4 v[12:13], off
	v_lshl_add_u64 v[12:13], v[16:17], 0, s[42:43]
	s_mov_b32 m0, s40
	s_add_u32 s4, s0, 0xb0080
	global_load_lds_dwordx4 v[12:13], off
	v_lshl_add_u64 v[12:13], v[18:19], 0, s[42:43]
	s_mov_b32 m0, s41
	s_addc_u32 s5, s1, 0
	global_load_lds_dwordx4 v[12:13], off
	s_add_i32 m0, s35, 0x1c000
	v_lshl_add_u64 v[12:13], s[4:5], 0, v[2:3]
	global_load_lds_dwordx4 v[12:13], off
	v_lshl_add_u64 v[12:13], s[4:5], 0, v[136:137]
	s_add_i32 m0, s35, 0x1e000
	s_movk_i32 s8, 0xb00
	global_load_lds_dwordx4 v[12:13], off
	s_waitcnt vmcnt(8)
	s_barrier
	v_lshrrev_b32_e32 v12, 1, v4
	v_mul_lo_u32 v4, v6, s8
	s_mov_b32 s9, 0xb000
	v_mad_u64_u32 v[12:13], s[4:5], v12, s9, v[4:5]
	v_or_b32_e32 v4, v12, v5
	v_add_lshl_u32 v138, v4, v7, 1
	v_lshrrev_b32_e32 v5, 1, v8
	v_mul_lo_u32 v4, v10, s8
	v_mad_u64_u32 v[4:5], s[4:5], v5, s9, v[4:5]
	s_waitcnt vmcnt(6)
	v_or_b32_e32 v4, v4, v9
	v_add_lshl_u32 v140, v4, v11, 1
	v_mov_b32_e32 v4, 0
	v_or_b32_e32 v228, s24, v147
	v_mov_b32_e32 v139, v3
	v_mov_b32_e32 v141, v3
	s_mov_b32 s56, 0
	v_add_u32_e32 v149, 0, v22
	v_mov_b32_e32 v5, v4
	v_mov_b32_e32 v6, v4
	v_mov_b32_e32 v7, v4
	v_mov_b32_e32 v8, v4
	v_mov_b32_e32 v9, v4
	v_mov_b32_e32 v10, v4
	v_mov_b32_e32 v11, v4
	v_mov_b32_e32 v20, v4
	v_mov_b32_e32 v21, v4
	v_mov_b32_e32 v22, v4
	v_mov_b32_e32 v23, v4
	v_mov_b32_e32 v24, v4
	v_mov_b32_e32 v25, v4
	v_mov_b32_e32 v26, v4
	v_mov_b32_e32 v27, v4
	v_mov_b32_e32 v36, v4
	v_mov_b32_e32 v37, v4
	v_mov_b32_e32 v38, v4
	v_mov_b32_e32 v39, v4
	v_mov_b32_e32 v40, v4
	v_mov_b32_e32 v41, v4
	v_mov_b32_e32 v42, v4
	v_mov_b32_e32 v43, v4
	v_mov_b32_e32 v52, v4
	v_mov_b32_e32 v53, v4
	v_mov_b32_e32 v54, v4
	v_mov_b32_e32 v55, v4
	v_mov_b32_e32 v56, v4
	v_mov_b32_e32 v57, v4
	v_mov_b32_e32 v58, v4
	v_mov_b32_e32 v59, v4
	v_mov_b32_e32 v12, v4
	v_mov_b32_e32 v13, v4
	v_mov_b32_e32 v14, v4
	v_mov_b32_e32 v15, v4
	v_mov_b32_e32 v16, v4
	v_mov_b32_e32 v17, v4
	v_mov_b32_e32 v18, v4
	v_mov_b32_e32 v19, v4
	v_mov_b32_e32 v28, v4
	v_mov_b32_e32 v29, v4
	s_waitcnt lgkmcnt(0)
	v_mov_b32_e32 v30, v4
	v_mov_b32_e32 v31, v4
	v_mov_b32_e32 v32, v4
	v_mov_b32_e32 v33, v4
	v_mov_b32_e32 v34, v4
	v_mov_b32_e32 v35, v4
	v_mov_b32_e32 v44, v4
	v_mov_b32_e32 v45, v4
	v_mov_b32_e32 v46, v4
	v_mov_b32_e32 v47, v4
	v_mov_b32_e32 v48, v4
	v_mov_b32_e32 v49, v4
	v_mov_b32_e32 v50, v4
	v_mov_b32_e32 v51, v4
	v_mov_b32_e32 v60, v4
	v_mov_b32_e32 v61, v4
	v_mov_b32_e32 v62, v4
	v_mov_b32_e32 v63, v4
	v_mov_b32_e32 v64, v4
	v_mov_b32_e32 v65, v4
	v_mov_b32_e32 v66, v4
	v_mov_b32_e32 v67, v4
	v_mov_b32_e32 v68, v4
	v_mov_b32_e32 v69, v4
	v_mov_b32_e32 v70, v4
	v_mov_b32_e32 v71, v4
	v_mov_b32_e32 v72, v4
	v_mov_b32_e32 v73, v4
	v_mov_b32_e32 v74, v4
	v_mov_b32_e32 v75, v4
	v_mov_b32_e32 v84, v4
	v_mov_b32_e32 v85, v4
	v_mov_b32_e32 v86, v4
	v_mov_b32_e32 v87, v4
	v_mov_b32_e32 v88, v4
	v_mov_b32_e32 v89, v4
	v_mov_b32_e32 v90, v4
	v_mov_b32_e32 v91, v4
	v_mov_b32_e32 v100, v4
	v_mov_b32_e32 v101, v4
	v_mov_b32_e32 v102, v4
	v_mov_b32_e32 v103, v4
	v_mov_b32_e32 v104, v4
	v_mov_b32_e32 v105, v4
	v_mov_b32_e32 v106, v4
	v_mov_b32_e32 v107, v4
	v_mov_b32_e32 v116, v4
	v_mov_b32_e32 v117, v4
	v_mov_b32_e32 v118, v4
	v_mov_b32_e32 v119, v4
	v_mov_b32_e32 v120, v4
	v_mov_b32_e32 v121, v4
	v_mov_b32_e32 v122, v4
	v_mov_b32_e32 v123, v4
	v_mov_b32_e32 v76, v4
	v_mov_b32_e32 v77, v4
	v_mov_b32_e32 v78, v4
	v_mov_b32_e32 v79, v4
	v_mov_b32_e32 v80, v4
	v_mov_b32_e32 v81, v4
	v_mov_b32_e32 v82, v4
	v_mov_b32_e32 v83, v4
	v_mov_b32_e32 v92, v4
	v_mov_b32_e32 v93, v4
	v_mov_b32_e32 v94, v4
	v_mov_b32_e32 v95, v4
	v_mov_b32_e32 v96, v4
	v_mov_b32_e32 v97, v4
	v_mov_b32_e32 v98, v4
	v_mov_b32_e32 v99, v4
	v_mov_b32_e32 v108, v4
	v_mov_b32_e32 v109, v4
	v_mov_b32_e32 v110, v4
	v_mov_b32_e32 v111, v4
	v_mov_b32_e32 v112, v4
	v_mov_b32_e32 v113, v4
	v_mov_b32_e32 v114, v4
	v_mov_b32_e32 v115, v4
	v_mov_b32_e32 v124, v4
	v_mov_b32_e32 v125, v4
	v_mov_b32_e32 v126, v4
	v_mov_b32_e32 v127, v4
	v_mov_b32_e32 v128, v4
	v_mov_b32_e32 v129, v4
	v_mov_b32_e32 v130, v4
	v_mov_b32_e32 v131, v4
	s_barrier
